# unit entry runs the loop-header set-up and branches straight to the peeled first K-step; the per-iteration first-iteration compare+branch at the top of the four loop bodies removed
# speedup vs baseline: 1.0028x; 1.0028x over previous
.Lp1_entry:
	s_cmpk_eq_i32 s66, 0xf00
	s_cselect_b64 s[68:69], -1, 0
	s_cmpk_lg_i32 s66, 0xf00
	v_mov_b32_e32 v160, v134
	v_mov_b32_e32 v162, v132
	v_mov_b32_e32 v164, v130
	v_mov_b32_e32 v166, v146
	s_branch .Lp1_first
.LBB0_101:
	ds_read_b128 v[184:187], v175
	ds_read_b128 v[188:191], v176
	ds_read_b128 v[192:195], v175 offset:2048
	ds_read_b128 v[196:199], v176 offset:2048
	ds_read_b128 v[200:203], v175 offset:16384
	ds_read_b128 v[204:207], v176 offset:16384
	ds_read_b128 v[208:211], v175 offset:18432
	ds_read_b128 v[212:215], v176 offset:18432
	s_add_u32 vcc_lo, s98, s66
	s_addc_u32 vcc_hi, s99, s67
	s_add_i32 m0, s77, 0x8000
	ds_read_b128 v[216:219], v178
	ds_read_b128 v[220:223], v178 offset:2048
	ds_read_b128 v[224:227], v179
	ds_read_b128 v[228:231], v179 offset:2048
	ds_read_b128 v[232:235], v178 offset:4096
	ds_read_b128 v[236:239], v178 offset:6144
	ds_read_b128 v[240:243], v179 offset:4096
	ds_read_b128 v[244:247], v179 offset:6144
	global_load_lds_dwordx4 v146, vcc
	s_add_i32 m0, s77, 0xa000
	s_nop 0
	global_load_lds_dwordx4 v130, vcc
	s_add_i32 m0, s77, 0xc000
	s_nop 0
	global_load_lds_dwordx4 v132, vcc
	s_add_i32 m0, s77, 0xe000
	s_nop 0
	global_load_lds_dwordx4 v134, vcc
	s_waitcnt vmcnt(8)
	s_waitcnt lgkmcnt(0)
	s_barrier
	s_setprio 1
	s_waitcnt lgkmcnt(0)
	v_mfma_f32_16x16x32_bf16 v[126:129], v[184:187], v[216:219], v[126:129]
	s_add_u32 s70, s64, s66
	s_addc_u32 s71, s65, s67
	s_add_u32 s73, s70, 0x100
	s_addc_u32 vcc_lo, s71, 0
	v_mfma_f32_16x16x32_bf16 v[122:125], v[192:195], v[216:219], v[122:125]
	s_and_b64 s[70:71], s[68:69], exec
	s_cselect_b32 s71, s47, vcc_lo
	s_cselect_b32 s70, s46, s73
	s_add_u32 s73, s15, s66
	v_mfma_f32_16x16x32_bf16 v[118:121], v[184:187], v[220:223], v[118:121]
	s_addc_u32 vcc_lo, s43, s67
	s_and_b64 s[68:69], s[68:69], exec
	s_cselect_b32 s69, s45, vcc_lo
	s_cselect_b32 s68, s44, s73
	v_mfma_f32_16x16x32_bf16 v[114:117], v[192:195], v[220:223], v[114:117]
	v_mfma_f32_16x16x32_bf16 v[110:113], v[184:187], v[232:235], v[110:113]
	v_mfma_f32_16x16x32_bf16 v[106:109], v[192:195], v[232:235], v[106:109]
	v_mfma_f32_16x16x32_bf16 v[102:105], v[184:187], v[236:239], v[102:105]
	v_mfma_f32_16x16x32_bf16 v[98:101], v[192:195], v[236:239], v[98:101]
	v_mfma_f32_16x16x32_bf16 v[126:129], v[188:191], v[224:227], v[126:129]
	v_mfma_f32_16x16x32_bf16 v[122:125], v[196:199], v[224:227], v[122:125]
	v_mfma_f32_16x16x32_bf16 v[118:121], v[188:191], v[228:231], v[118:121]
	v_mfma_f32_16x16x32_bf16 v[114:117], v[196:199], v[228:231], v[114:117]
	v_mfma_f32_16x16x32_bf16 v[110:113], v[188:191], v[240:243], v[110:113]
	v_mfma_f32_16x16x32_bf16 v[106:109], v[196:199], v[240:243], v[106:109]
	v_mfma_f32_16x16x32_bf16 v[102:105], v[188:191], v[244:247], v[102:105]
	v_mfma_f32_16x16x32_bf16 v[98:101], v[196:199], v[244:247], v[98:101]
	s_setprio 0
	s_setprio 1
	v_mfma_f32_16x16x32_bf16 v[62:65], v[200:203], v[216:219], v[62:65]
	v_mfma_f32_16x16x32_bf16 v[58:61], v[208:211], v[216:219], v[58:61]
	v_mfma_f32_16x16x32_bf16 v[54:57], v[200:203], v[220:223], v[54:57]
	v_mfma_f32_16x16x32_bf16 v[50:53], v[208:211], v[220:223], v[50:53]
	v_mfma_f32_16x16x32_bf16 v[46:49], v[200:203], v[232:235], v[46:49]
	v_mfma_f32_16x16x32_bf16 v[42:45], v[208:211], v[232:235], v[42:45]
	v_mfma_f32_16x16x32_bf16 v[38:41], v[200:203], v[236:239], v[38:41]
	v_mfma_f32_16x16x32_bf16 v[34:37], v[208:211], v[236:239], v[34:37]
	v_mfma_f32_16x16x32_bf16 v[62:65], v[204:207], v[224:227], v[62:65]
	v_mfma_f32_16x16x32_bf16 v[58:61], v[212:215], v[224:227], v[58:61]
	v_mfma_f32_16x16x32_bf16 v[54:57], v[204:207], v[228:231], v[54:57]
	v_mfma_f32_16x16x32_bf16 v[50:53], v[212:215], v[228:231], v[50:53]
	v_mfma_f32_16x16x32_bf16 v[46:49], v[204:207], v[240:243], v[46:49]
	v_mfma_f32_16x16x32_bf16 v[42:45], v[212:215], v[240:243], v[42:45]
	v_mfma_f32_16x16x32_bf16 v[38:41], v[204:207], v[244:247], v[38:41]
	v_mfma_f32_16x16x32_bf16 v[34:37], v[212:215], v[244:247], v[34:37]
	s_setprio 0
	s_barrier
	s_add_i32 s73, s87, s76
	s_mov_b32 m0, s73
	ds_read_b128 v[216:219], v178 offset:16384
	ds_read_b128 v[220:223], v178 offset:18432
	ds_read_b128 v[224:227], v179 offset:16384
	ds_read_b128 v[228:231], v179 offset:18432
	ds_read_b128 v[232:235], v178 offset:20480
	ds_read_b128 v[236:239], v178 offset:22528
	ds_read_b128 v[240:243], v179 offset:20480
	ds_read_b128 v[244:247], v179 offset:22528
	global_load_lds_dwordx4 v142, s[68:69]
	s_add_i32 m0, s73, 0x2000
	s_add_u32 vcc_lo, s68, 0x80000
	s_addc_u32 vcc_hi, s69, 0
	s_add_i32 s73, s89, s76
	global_load_lds_dwordx4 v144, s[68:69]
	s_mov_b32 m0, s73
	s_nop 0
	global_load_lds_dwordx4 v142, vcc
	s_add_i32 m0, s73, 0x2000
	s_nop 0
	global_load_lds_dwordx4 v144, vcc
	s_waitcnt vmcnt(6)
	s_waitcnt lgkmcnt(0)
	s_barrier
	s_setprio 1
	s_waitcnt lgkmcnt(0)
	v_mfma_f32_16x16x32_bf16 v[94:97], v[184:187], v[216:219], v[94:97]
	v_mfma_f32_16x16x32_bf16 v[90:93], v[192:195], v[216:219], v[90:93]
	v_mfma_f32_16x16x32_bf16 v[86:89], v[184:187], v[220:223], v[86:89]
	v_mfma_f32_16x16x32_bf16 v[82:85], v[192:195], v[220:223], v[82:85]
	v_mfma_f32_16x16x32_bf16 v[78:81], v[184:187], v[232:235], v[78:81]
	v_mfma_f32_16x16x32_bf16 v[74:77], v[192:195], v[232:235], v[74:77]
	v_mfma_f32_16x16x32_bf16 v[70:73], v[184:187], v[236:239], v[70:73]
	v_mfma_f32_16x16x32_bf16 v[66:69], v[192:195], v[236:239], v[66:69]
	v_mfma_f32_16x16x32_bf16 v[94:97], v[188:191], v[224:227], v[94:97]
	v_mfma_f32_16x16x32_bf16 v[90:93], v[196:199], v[224:227], v[90:93]
	v_mfma_f32_16x16x32_bf16 v[86:89], v[188:191], v[228:231], v[86:89]
	v_mfma_f32_16x16x32_bf16 v[82:85], v[196:199], v[228:231], v[82:85]
	v_mfma_f32_16x16x32_bf16 v[78:81], v[188:191], v[240:243], v[78:81]
	v_mfma_f32_16x16x32_bf16 v[74:77], v[196:199], v[240:243], v[74:77]
	v_mfma_f32_16x16x32_bf16 v[70:73], v[188:191], v[244:247], v[70:73]
	v_mfma_f32_16x16x32_bf16 v[66:69], v[196:199], v[244:247], v[66:69]
	s_setprio 0
	s_setprio 1
	v_mfma_f32_16x16x32_bf16 v[30:33], v[200:203], v[216:219], v[30:33]
	v_mfma_f32_16x16x32_bf16 v[26:29], v[208:211], v[216:219], v[26:29]
	v_mfma_f32_16x16x32_bf16 v[22:25], v[200:203], v[220:223], v[22:25]
	v_mfma_f32_16x16x32_bf16 v[18:21], v[208:211], v[220:223], v[18:21]
	v_mfma_f32_16x16x32_bf16 v[14:17], v[200:203], v[232:235], v[14:17]
	v_mfma_f32_16x16x32_bf16 v[10:13], v[208:211], v[232:235], v[10:13]
	v_mfma_f32_16x16x32_bf16 v[6:9], v[200:203], v[236:239], v[6:9]
	v_mfma_f32_16x16x32_bf16 v[2:5], v[208:211], v[236:239], v[2:5]
	v_mfma_f32_16x16x32_bf16 v[30:33], v[204:207], v[224:227], v[30:33]
	v_mfma_f32_16x16x32_bf16 v[26:29], v[212:215], v[224:227], v[26:29]
	v_mfma_f32_16x16x32_bf16 v[22:25], v[204:207], v[228:231], v[22:25]
	v_mfma_f32_16x16x32_bf16 v[18:21], v[212:215], v[228:231], v[18:21]
	v_mfma_f32_16x16x32_bf16 v[14:17], v[204:207], v[240:243], v[14:17]
	v_mfma_f32_16x16x32_bf16 v[10:13], v[212:215], v[240:243], v[10:13]
	v_mfma_f32_16x16x32_bf16 v[6:9], v[204:207], v[244:247], v[6:9]
	v_mfma_f32_16x16x32_bf16 v[2:5], v[212:215], v[244:247], v[2:5]
	s_setprio 0
	s_barrier

.Lp3_entry:
	s_cmpk_eq_i32 s28, 0xf00
	s_cselect_b64 s[30:31], -1, 0
	s_cmpk_lg_i32 s28, 0xf00
	v_mov_b32_e32 v160, v134
	v_mov_b32_e32 v162, v132
	v_mov_b32_e32 v164, v130
	v_mov_b32_e32 v166, v150
	s_branch .Lp3_first
.LBB0_385:
	ds_read_b128 v[184:187], v174
	ds_read_b128 v[188:191], v175
	ds_read_b128 v[192:195], v174 offset:2048
	ds_read_b128 v[196:199], v175 offset:2048
	ds_read_b128 v[200:203], v174 offset:16384
	ds_read_b128 v[204:207], v175 offset:16384
	ds_read_b128 v[208:211], v174 offset:18432
	ds_read_b128 v[212:215], v175 offset:18432
	v_lshl_add_u64 v[248:249], v[158:159], 0, s[28:29]
	s_add_i32 m0, s39, 0x8000
	ds_read_b128 v[216:219], v177
	ds_read_b128 v[220:223], v177 offset:2048
	ds_read_b128 v[224:227], v178
	ds_read_b128 v[228:231], v178 offset:2048
	ds_read_b128 v[232:235], v177 offset:4096
	ds_read_b128 v[236:239], v177 offset:6144
	ds_read_b128 v[240:243], v178 offset:4096
	ds_read_b128 v[244:247], v178 offset:6144
	global_load_lds_dwordx4 v[248:249], off
	v_lshl_add_u64 v[248:249], v[156:157], 0, s[28:29]
	s_add_i32 m0, s39, 0xa000
	s_nop 0
	global_load_lds_dwordx4 v[248:249], off
	v_lshl_add_u64 v[248:249], v[154:155], 0, s[28:29]
	s_add_i32 m0, s39, 0xc000
	s_nop 0
	global_load_lds_dwordx4 v[248:249], off
	v_lshl_add_u64 v[248:249], v[144:145], 0, s[28:29]
	s_add_i32 m0, s39, 0xe000
	s_nop 0
	global_load_lds_dwordx4 v[248:249], off
	s_waitcnt vmcnt(8)
	s_waitcnt lgkmcnt(0)
	s_barrier
	s_setprio 1
	s_waitcnt lgkmcnt(0)
	v_mfma_f32_16x16x32_bf16 v[126:129], v[184:187], v[216:219], v[126:129]
	s_add_u32 s34, s2, s28
	s_addc_u32 s35, s3, s29
	s_add_u32 s77, s34, 0x63000100
	s_addc_u32 s78, s35, 0
	v_mfma_f32_16x16x32_bf16 v[122:125], v[192:195], v[216:219], v[122:125]
	s_and_b64 s[34:35], s[30:31], exec
	s_cselect_b32 s35, s7, s78
	s_cselect_b32 s34, s6, s77
	s_add_u32 s77, s25, s28
	v_mfma_f32_16x16x32_bf16 v[118:121], v[184:187], v[220:223], v[118:121]
	s_addc_u32 s78, s75, s29
	s_and_b64 s[30:31], s[30:31], exec
	s_cselect_b32 s31, s27, s78
	s_cselect_b32 s30, s26, s77
	v_mfma_f32_16x16x32_bf16 v[114:117], v[192:195], v[220:223], v[114:117]
	v_mfma_f32_16x16x32_bf16 v[110:113], v[184:187], v[232:235], v[110:113]
	v_mfma_f32_16x16x32_bf16 v[102:105], v[192:195], v[232:235], v[102:105]
	v_mfma_f32_16x16x32_bf16 v[94:97], v[184:187], v[236:239], v[94:97]
	v_mfma_f32_16x16x32_bf16 v[86:89], v[192:195], v[236:239], v[86:89]
	v_mfma_f32_16x16x32_bf16 v[126:129], v[188:191], v[224:227], v[126:129]
	v_mfma_f32_16x16x32_bf16 v[122:125], v[196:199], v[224:227], v[122:125]
	v_mfma_f32_16x16x32_bf16 v[118:121], v[188:191], v[228:231], v[118:121]
	v_mfma_f32_16x16x32_bf16 v[114:117], v[196:199], v[228:231], v[114:117]
	v_mfma_f32_16x16x32_bf16 v[110:113], v[188:191], v[240:243], v[110:113]
	v_mfma_f32_16x16x32_bf16 v[102:105], v[196:199], v[240:243], v[102:105]
	v_mfma_f32_16x16x32_bf16 v[94:97], v[188:191], v[244:247], v[94:97]
	v_mfma_f32_16x16x32_bf16 v[86:89], v[196:199], v[244:247], v[86:89]
	s_setprio 0
	s_setprio 1
	v_mfma_f32_16x16x32_bf16 v[106:109], v[200:203], v[216:219], v[106:109]
	v_mfma_f32_16x16x32_bf16 v[98:101], v[208:211], v[216:219], v[98:101]
	v_mfma_f32_16x16x32_bf16 v[90:93], v[200:203], v[220:223], v[90:93]
	v_mfma_f32_16x16x32_bf16 v[82:85], v[208:211], v[220:223], v[82:85]
	v_mfma_f32_16x16x32_bf16 v[78:81], v[200:203], v[232:235], v[78:81]
	v_mfma_f32_16x16x32_bf16 v[74:77], v[208:211], v[232:235], v[74:77]
	v_mfma_f32_16x16x32_bf16 v[70:73], v[200:203], v[236:239], v[70:73]
	v_mfma_f32_16x16x32_bf16 v[66:69], v[208:211], v[236:239], v[66:69]
	v_mfma_f32_16x16x32_bf16 v[106:109], v[204:207], v[224:227], v[106:109]
	v_mfma_f32_16x16x32_bf16 v[98:101], v[212:215], v[224:227], v[98:101]
	v_mfma_f32_16x16x32_bf16 v[90:93], v[204:207], v[228:231], v[90:93]
	v_mfma_f32_16x16x32_bf16 v[82:85], v[212:215], v[228:231], v[82:85]
	v_mfma_f32_16x16x32_bf16 v[78:81], v[204:207], v[240:243], v[78:81]
	v_mfma_f32_16x16x32_bf16 v[74:77], v[212:215], v[240:243], v[74:77]
	v_mfma_f32_16x16x32_bf16 v[70:73], v[204:207], v[244:247], v[70:73]
	v_mfma_f32_16x16x32_bf16 v[66:69], v[212:215], v[244:247], v[66:69]
	s_setprio 0
	s_barrier
	s_add_i32 s77, s45, s33
	v_lshl_add_u64 v[248:249], s[30:31], 0, v[146:147]
	s_mov_b32 m0, s77
	ds_read_b128 v[216:219], v177 offset:16384
	ds_read_b128 v[220:223], v177 offset:18432
	ds_read_b128 v[224:227], v178 offset:16384
	ds_read_b128 v[228:231], v178 offset:18432
	ds_read_b128 v[232:235], v177 offset:20480
	ds_read_b128 v[236:239], v177 offset:22528
	ds_read_b128 v[240:243], v178 offset:20480
	ds_read_b128 v[244:247], v178 offset:22528
	global_load_lds_dwordx4 v[248:249], off
	s_add_i32 m0, s77, 0x2000
	s_add_u32 s78, s30, 0x80000
	v_lshl_add_u64 v[250:251], s[30:31], 0, v[148:149]
	s_addc_u32 s79, s31, 0
	s_add_i32 s77, s47, s33
	global_load_lds_dwordx4 v[250:251], off
	s_mov_b32 m0, s77
	s_nop 0
	global_load_lds_dwordx4 v146, s[78:79]
	s_add_i32 m0, s77, 0x2000
	s_nop 0
	global_load_lds_dwordx4 v148, s[78:79]
	s_waitcnt vmcnt(6)
	s_waitcnt lgkmcnt(0)
	s_barrier
	s_setprio 1
	s_waitcnt lgkmcnt(0)
	v_mfma_f32_16x16x32_bf16 v[62:65], v[184:187], v[216:219], v[62:65]
	v_mfma_f32_16x16x32_bf16 v[58:61], v[192:195], v[216:219], v[58:61]
	v_mfma_f32_16x16x32_bf16 v[50:53], v[184:187], v[220:223], v[50:53]
	v_mfma_f32_16x16x32_bf16 v[42:45], v[192:195], v[220:223], v[42:45]
	v_mfma_f32_16x16x32_bf16 v[34:37], v[184:187], v[232:235], v[34:37]
	v_mfma_f32_16x16x32_bf16 v[26:29], v[192:195], v[232:235], v[26:29]
	v_mfma_f32_16x16x32_bf16 v[18:21], v[184:187], v[236:239], v[18:21]
	v_mfma_f32_16x16x32_bf16 v[10:13], v[192:195], v[236:239], v[10:13]
	v_mfma_f32_16x16x32_bf16 v[62:65], v[188:191], v[224:227], v[62:65]
	v_mfma_f32_16x16x32_bf16 v[58:61], v[196:199], v[224:227], v[58:61]
	v_mfma_f32_16x16x32_bf16 v[50:53], v[188:191], v[228:231], v[50:53]
	v_mfma_f32_16x16x32_bf16 v[42:45], v[196:199], v[228:231], v[42:45]
	v_mfma_f32_16x16x32_bf16 v[34:37], v[188:191], v[240:243], v[34:37]
	v_mfma_f32_16x16x32_bf16 v[26:29], v[196:199], v[240:243], v[26:29]
	v_mfma_f32_16x16x32_bf16 v[18:21], v[188:191], v[244:247], v[18:21]
	v_mfma_f32_16x16x32_bf16 v[10:13], v[196:199], v[244:247], v[10:13]
	s_setprio 0
	s_setprio 1
	v_mfma_f32_16x16x32_bf16 v[54:57], v[200:203], v[216:219], v[54:57]
	v_mfma_f32_16x16x32_bf16 v[46:49], v[208:211], v[216:219], v[46:49]
	v_mfma_f32_16x16x32_bf16 v[38:41], v[200:203], v[220:223], v[38:41]
	v_mfma_f32_16x16x32_bf16 v[30:33], v[208:211], v[220:223], v[30:33]
	v_mfma_f32_16x16x32_bf16 v[22:25], v[200:203], v[232:235], v[22:25]
	v_mfma_f32_16x16x32_bf16 v[14:17], v[208:211], v[232:235], v[14:17]
	v_mfma_f32_16x16x32_bf16 v[6:9], v[200:203], v[236:239], v[6:9]
	v_mfma_f32_16x16x32_bf16 v[2:5], v[208:211], v[236:239], v[2:5]
	v_mfma_f32_16x16x32_bf16 v[54:57], v[204:207], v[224:227], v[54:57]
	v_mfma_f32_16x16x32_bf16 v[46:49], v[212:215], v[224:227], v[46:49]
	v_mfma_f32_16x16x32_bf16 v[38:41], v[204:207], v[228:231], v[38:41]
	v_mfma_f32_16x16x32_bf16 v[30:33], v[212:215], v[228:231], v[30:33]
	v_mfma_f32_16x16x32_bf16 v[22:25], v[204:207], v[240:243], v[22:25]
	v_mfma_f32_16x16x32_bf16 v[14:17], v[212:215], v[240:243], v[14:17]
	v_mfma_f32_16x16x32_bf16 v[6:9], v[204:207], v[244:247], v[6:9]
	v_mfma_f32_16x16x32_bf16 v[2:5], v[212:215], v[244:247], v[2:5]
	s_setprio 0
	s_barrier

.Lp6_entry:
	s_cmpk_eq_i32 s40, 0x700
	s_cselect_b64 s[42:43], -1, 0
	s_cmpk_lg_i32 s40, 0x700
	v_mov_b32_e32 v192, v182
	v_mov_b32_e32 v194, v180
	v_mov_b32_e32 v196, v178
	v_mov_b32_e32 v198, v176
	s_branch .Lp6_first
.LBB0_777:
	ds_read_b128 v[18:21], v208
	ds_read_b128 v[22:25], v209
	ds_read_b128 v[26:29], v208 offset:2048
	ds_read_b128 v[30:33], v209 offset:2048
	ds_read_b128 v[2:5], v208 offset:16384
	ds_read_b128 v[6:9], v209 offset:16384
	ds_read_b128 v[10:13], v208 offset:18432
	ds_read_b128 v[14:17], v209 offset:18432
	s_add_u32 s84, s18, s40
	s_addc_u32 s85, s19, s41
	s_add_i32 m0, s35, 0x8000
	ds_read_b128 v[218:221], v211
	ds_read_b128 v[226:229], v211 offset:2048
	ds_read_b128 v[222:225], v212
	ds_read_b128 v[230:233], v212 offset:2048
	ds_read_b128 v[234:237], v211 offset:4096
	ds_read_b128 v[242:245], v211 offset:6144
	ds_read_b128 v[238:241], v212 offset:4096
	ds_read_b128 v[246:249], v212 offset:6144
	global_load_lds_dwordx4 v176, s[84:85]
	s_add_i32 m0, s35, 0xa000
	s_nop 0
	global_load_lds_dwordx4 v178, s[84:85]
	s_add_i32 m0, s35, 0xc000
	s_nop 0
	global_load_lds_dwordx4 v180, s[84:85]
	s_add_i32 m0, s35, 0xe000
	s_nop 0
	global_load_lds_dwordx4 v182, s[84:85]
	s_waitcnt vmcnt(8)
	s_waitcnt lgkmcnt(0)
	s_barrier
	s_setprio 1
	s_waitcnt lgkmcnt(0)
	v_mfma_f32_16x16x128_f8f6f4 v[158:161], v[18:25], v[218:225], v[158:161]
	s_add_u32 s44, s2, s40
	s_addc_u32 s45, s3, s41
	s_add_u32 s84, s44, 0x56800100
	s_addc_u32 s85, s45, 0
	v_mfma_f32_16x16x128_f8f6f4 v[154:157], v[26:33], v[218:225], v[154:157]
	s_and_b64 s[44:45], s[42:43], exec
	s_cselect_b32 s45, s9, s85
	s_cselect_b32 s44, s8, s84
	s_add_u32 s84, s29, s40
	v_mfma_f32_16x16x128_f8f6f4 v[150:153], v[18:25], v[226:233], v[150:153]
	s_addc_u32 s85, s37, s41
	s_and_b64 s[42:43], s[42:43], exec
	s_cselect_b32 s43, s31, s85
	s_cselect_b32 s42, s30, s84
	v_mfma_f32_16x16x128_f8f6f4 v[146:149], v[26:33], v[226:233], v[146:149]
	v_mfma_f32_16x16x128_f8f6f4 v[126:129], v[18:25], v[234:241], v[126:129]
	v_mfma_f32_16x16x128_f8f6f4 v[122:125], v[26:33], v[234:241], v[122:125]
	v_mfma_f32_16x16x128_f8f6f4 v[110:113], v[18:25], v[242:249], v[110:113]
	v_mfma_f32_16x16x128_f8f6f4 v[106:109], v[26:33], v[242:249], v[106:109]
	s_setprio 0
	s_setprio 1
	v_mfma_f32_16x16x128_f8f6f4 v[142:145], v[2:9], v[218:225], v[142:145]
	v_mfma_f32_16x16x128_f8f6f4 v[138:141], v[10:17], v[218:225], v[138:141]
	v_mfma_f32_16x16x128_f8f6f4 v[134:137], v[2:9], v[226:233], v[134:137]
	v_mfma_f32_16x16x128_f8f6f4 v[130:133], v[10:17], v[226:233], v[130:133]
	v_mfma_f32_16x16x128_f8f6f4 v[118:121], v[2:9], v[234:241], v[118:121]
	v_mfma_f32_16x16x128_f8f6f4 v[114:117], v[10:17], v[234:241], v[114:117]
	v_mfma_f32_16x16x128_f8f6f4 v[102:105], v[2:9], v[242:249], v[102:105]
	v_mfma_f32_16x16x128_f8f6f4 v[98:101], v[10:17], v[242:249], v[98:101]
	s_setprio 0
	s_barrier
	s_add_i32 s84, s68, s33
	s_mov_b32 m0, s84
	ds_read_b128 v[218:221], v211 offset:16384
	ds_read_b128 v[226:229], v211 offset:18432
	ds_read_b128 v[222:225], v212 offset:16384
	ds_read_b128 v[230:233], v212 offset:18432
	ds_read_b128 v[234:237], v211 offset:20480
	ds_read_b128 v[242:245], v211 offset:22528
	ds_read_b128 v[238:241], v212 offset:20480
	ds_read_b128 v[246:249], v212 offset:22528
	global_load_lds_dwordx4 v164, s[42:43]
	s_add_i32 m0, s84, 0x2000
	s_add_u32 s84, s42, 0x40000
	s_addc_u32 s85, s43, 0
	s_add_i32 s86, s70, s33
	global_load_lds_dwordx4 v166, s[42:43]
	s_mov_b32 m0, s86
	s_nop 0
	global_load_lds_dwordx4 v164, s[84:85]
	s_add_i32 m0, s86, 0x2000
	s_nop 0
	global_load_lds_dwordx4 v166, s[84:85]
	s_waitcnt vmcnt(6)
	s_waitcnt lgkmcnt(0)
	s_barrier
	s_setprio 1
	s_waitcnt lgkmcnt(0)
	v_mfma_f32_16x16x128_f8f6f4 v[94:97], v[18:25], v[218:225], v[94:97]
	v_mfma_f32_16x16x128_f8f6f4 v[90:93], v[26:33], v[218:225], v[90:93]
	v_mfma_f32_16x16x128_f8f6f4 v[78:81], v[18:25], v[226:233], v[78:81]
	v_mfma_f32_16x16x128_f8f6f4 v[74:77], v[26:33], v[226:233], v[74:77]
	v_mfma_f32_16x16x128_f8f6f4 v[62:65], v[18:25], v[234:241], v[62:65]
	v_mfma_f32_16x16x128_f8f6f4 v[58:61], v[26:33], v[234:241], v[58:61]
	v_mfma_f32_16x16x128_f8f6f4 v[46:49], v[18:25], v[242:249], v[46:49]
	v_mfma_f32_16x16x128_f8f6f4 v[42:45], v[26:33], v[242:249], v[42:45]
	s_setprio 0
	s_setprio 1
	v_mfma_f32_16x16x128_f8f6f4 v[86:89], v[2:9], v[218:225], v[86:89]
	v_mfma_f32_16x16x128_f8f6f4 v[82:85], v[10:17], v[218:225], v[82:85]
	v_mfma_f32_16x16x128_f8f6f4 v[70:73], v[2:9], v[226:233], v[70:73]
	v_mfma_f32_16x16x128_f8f6f4 v[66:69], v[10:17], v[226:233], v[66:69]
	v_mfma_f32_16x16x128_f8f6f4 v[54:57], v[2:9], v[234:241], v[54:57]
	v_mfma_f32_16x16x128_f8f6f4 v[50:53], v[10:17], v[234:241], v[50:53]
	v_mfma_f32_16x16x128_f8f6f4 v[38:41], v[2:9], v[242:249], v[38:41]
	v_mfma_f32_16x16x128_f8f6f4 v[34:37], v[10:17], v[242:249], v[34:37]
	s_setprio 0
	s_barrier

.Lp7_entry:
	s_cmpk_eq_i32 s44, 0x700
	s_cselect_b64 s[46:47], -1, 0
	s_cmpk_lg_i32 s44, 0x700
	v_mov_b32_e32 v192, v174
	v_mov_b32_e32 v194, v172
	v_mov_b32_e32 v196, v170
	v_mov_b32_e32 v198, v166
	s_branch .Lp7_first
.LBB0_862:
	ds_read_b128 v[18:21], v210
	ds_read_b128 v[22:25], v211
	ds_read_b128 v[26:29], v210 offset:2048
	ds_read_b128 v[30:33], v211 offset:2048
	ds_read_b128 v[2:5], v210 offset:16384
	ds_read_b128 v[6:9], v211 offset:16384
	ds_read_b128 v[10:13], v210 offset:18432
	ds_read_b128 v[14:17], v211 offset:18432
	s_add_u32 s82, s20, s44
	s_addc_u32 s83, s21, s45
	s_add_i32 m0, s41, 0x8000
	ds_read_b128 v[220:223], v213
	ds_read_b128 v[228:231], v213 offset:2048
	ds_read_b128 v[224:227], v214
	ds_read_b128 v[232:235], v214 offset:2048
	ds_read_b128 v[236:239], v213 offset:4096
	ds_read_b128 v[244:247], v213 offset:6144
	ds_read_b128 v[240:243], v214 offset:4096
	ds_read_b128 v[248:251], v214 offset:6144
	global_load_lds_dwordx4 v166, s[82:83]
	s_add_i32 m0, s41, 0xa000
	s_nop 0
	global_load_lds_dwordx4 v170, s[82:83]
	s_add_i32 m0, s41, 0xc000
	s_nop 0
	global_load_lds_dwordx4 v172, s[82:83]
	s_add_i32 m0, s41, 0xe000
	s_nop 0
	global_load_lds_dwordx4 v174, s[82:83]
	s_waitcnt vmcnt(8)
	s_waitcnt lgkmcnt(0)
	s_barrier
	s_setprio 1
	s_waitcnt lgkmcnt(0)
	v_mfma_f32_16x16x128_f8f6f4 v[158:161], v[18:25], v[220:227], v[158:161]
	s_add_u32 s48, s2, s44
	s_addc_u32 s49, s3, s45
	s_add_u32 s81, s48, 0x3e800100
	s_addc_u32 s82, s49, 0
	v_mfma_f32_16x16x128_f8f6f4 v[154:157], v[26:33], v[220:227], v[154:157]
	s_and_b64 s[48:49], s[46:47], exec
	s_cselect_b32 s49, s9, s82
	s_cselect_b32 s48, s8, s81
	s_add_u32 s81, s35, s44
	v_mfma_f32_16x16x128_f8f6f4 v[150:153], v[18:25], v[228:235], v[150:153]
	s_addc_u32 s82, s37, s45
	s_and_b64 s[46:47], s[46:47], exec
	s_cselect_b32 s47, s39, s82
	s_cselect_b32 s46, s38, s81
	v_mfma_f32_16x16x128_f8f6f4 v[146:149], v[26:33], v[228:235], v[146:149]
	v_mfma_f32_16x16x128_f8f6f4 v[142:145], v[18:25], v[236:243], v[142:145]
	v_mfma_f32_16x16x128_f8f6f4 v[138:141], v[26:33], v[236:243], v[138:141]
	v_mfma_f32_16x16x128_f8f6f4 v[134:137], v[18:25], v[244:251], v[134:137]
	v_mfma_f32_16x16x128_f8f6f4 v[130:133], v[26:33], v[244:251], v[130:133]
	s_setprio 0
	s_setprio 1
	v_mfma_f32_16x16x128_f8f6f4 v[102:105], v[2:9], v[220:227], v[102:105]
	v_mfma_f32_16x16x128_f8f6f4 v[94:97], v[10:17], v[220:227], v[94:97]
	v_mfma_f32_16x16x128_f8f6f4 v[86:89], v[2:9], v[228:235], v[86:89]
	v_mfma_f32_16x16x128_f8f6f4 v[82:85], v[10:17], v[228:235], v[82:85]
	v_mfma_f32_16x16x128_f8f6f4 v[78:81], v[2:9], v[236:243], v[78:81]
	v_mfma_f32_16x16x128_f8f6f4 v[74:77], v[10:17], v[236:243], v[74:77]
	v_mfma_f32_16x16x128_f8f6f4 v[70:73], v[2:9], v[244:251], v[70:73]
	v_mfma_f32_16x16x128_f8f6f4 v[66:69], v[10:17], v[244:251], v[66:69]
	s_setprio 0
	s_barrier
	s_add_i32 s81, s66, s51
	s_mov_b32 m0, s81
	ds_read_b128 v[220:223], v213 offset:16384
	ds_read_b128 v[228:231], v213 offset:18432
	ds_read_b128 v[224:227], v214 offset:16384
	ds_read_b128 v[232:235], v214 offset:18432
	ds_read_b128 v[236:239], v213 offset:20480
	ds_read_b128 v[244:247], v213 offset:22528
	ds_read_b128 v[240:243], v214 offset:20480
	ds_read_b128 v[248:251], v214 offset:22528
	global_load_lds_dwordx4 v162, s[46:47]
	s_add_i32 m0, s81, 0x2000
	s_add_u32 s82, s46, 0x40000
	s_addc_u32 s83, s47, 0
	s_add_i32 s81, s68, s51
	global_load_lds_dwordx4 v164, s[46:47]
	s_mov_b32 m0, s81
	s_nop 0
	global_load_lds_dwordx4 v162, s[82:83]
	s_add_i32 m0, s81, 0x2000
	s_nop 0
	global_load_lds_dwordx4 v164, s[82:83]
	s_waitcnt vmcnt(6)
	s_waitcnt lgkmcnt(0)
	s_barrier
	s_setprio 1
	s_waitcnt lgkmcnt(0)
	v_mfma_f32_16x16x128_f8f6f4 v[126:129], v[18:25], v[220:227], v[126:129]
	v_mfma_f32_16x16x128_f8f6f4 v[122:125], v[26:33], v[220:227], v[122:125]
	v_mfma_f32_16x16x128_f8f6f4 v[118:121], v[18:25], v[228:235], v[118:121]
	v_mfma_f32_16x16x128_f8f6f4 v[114:117], v[26:33], v[228:235], v[114:117]
	v_mfma_f32_16x16x128_f8f6f4 v[110:113], v[18:25], v[236:243], v[110:113]
	v_mfma_f32_16x16x128_f8f6f4 v[106:109], v[26:33], v[236:243], v[106:109]
	v_mfma_f32_16x16x128_f8f6f4 v[98:101], v[18:25], v[244:251], v[98:101]
	v_mfma_f32_16x16x128_f8f6f4 v[90:93], v[26:33], v[244:251], v[90:93]
	s_setprio 0
	s_setprio 1
	v_mfma_f32_16x16x128_f8f6f4 v[62:65], v[2:9], v[220:227], v[62:65]
	v_mfma_f32_16x16x128_f8f6f4 v[58:61], v[10:17], v[220:227], v[58:61]
	v_mfma_f32_16x16x128_f8f6f4 v[54:57], v[2:9], v[228:235], v[54:57]
	v_mfma_f32_16x16x128_f8f6f4 v[50:53], v[10:17], v[228:235], v[50:53]
	v_mfma_f32_16x16x128_f8f6f4 v[46:49], v[2:9], v[236:243], v[46:49]
	v_mfma_f32_16x16x128_f8f6f4 v[42:45], v[10:17], v[236:243], v[42:45]
	v_mfma_f32_16x16x128_f8f6f4 v[38:41], v[2:9], v[244:251], v[38:41]
	v_mfma_f32_16x16x128_f8f6f4 v[34:37], v[10:17], v[244:251], v[34:37]
	s_setprio 0
	s_barrier
